# P7 router weight image: 17 loads in one batch instead of five load/wait/write rounds
# speedup vs baseline: 1.0025x; 1.0025x over previous
.LBB0_925:
	s_or_b64 exec, exec, s[0:1]
	s_add_u32 s0, s92, 0x140000
	s_addc_u32 s1, s93, 0
	v_lshl_add_u32 v1, v2, 4, 0
	s_movk_i32 s2, 0xf800
	s_waitcnt lgkmcnt(0)
	s_waitcnt vmcnt(0)
	v_lshlrev_b32_e32 v3, 4, v2
	v_cmp_gt_i32_e32 vcc, 64, v2
	s_add_u32 s98, s0, 0x20000
	s_addc_u32 s99, s1, 0
	s_and_saveexec_b64 s[2:3], vcc
	s_cbranch_execz .Lp7_notail
	global_load_dwordx4 v[68:71], v3, s[98:99]
.Lp7_notail:
	s_or_b64 exec, exec, s[2:3]
	s_mov_b64 s[98:99], s[0:1]
	global_load_dwordx4 v[4:7], v3, s[98:99]
	s_add_u32 s98, s98, 0x2000
	s_addc_u32 s99, s99, 0
	global_load_dwordx4 v[8:11], v3, s[98:99]
	s_add_u32 s98, s98, 0x2000
	s_addc_u32 s99, s99, 0
	global_load_dwordx4 v[12:15], v3, s[98:99]
	s_add_u32 s98, s98, 0x2000
	s_addc_u32 s99, s99, 0
	global_load_dwordx4 v[16:19], v3, s[98:99]
	s_add_u32 s98, s98, 0x2000
	s_addc_u32 s99, s99, 0
	global_load_dwordx4 v[20:23], v3, s[98:99]
	s_add_u32 s98, s98, 0x2000
	s_addc_u32 s99, s99, 0
	global_load_dwordx4 v[24:27], v3, s[98:99]
	s_add_u32 s98, s98, 0x2000
	s_addc_u32 s99, s99, 0
	global_load_dwordx4 v[28:31], v3, s[98:99]
	s_add_u32 s98, s98, 0x2000
	s_addc_u32 s99, s99, 0
	global_load_dwordx4 v[32:35], v3, s[98:99]
	s_add_u32 s98, s98, 0x2000
	s_addc_u32 s99, s99, 0
	global_load_dwordx4 v[36:39], v3, s[98:99]
	s_add_u32 s98, s98, 0x2000
	s_addc_u32 s99, s99, 0
	global_load_dwordx4 v[40:43], v3, s[98:99]
	s_add_u32 s98, s98, 0x2000
	s_addc_u32 s99, s99, 0
	global_load_dwordx4 v[44:47], v3, s[98:99]
	s_add_u32 s98, s98, 0x2000
	s_addc_u32 s99, s99, 0
	global_load_dwordx4 v[48:51], v3, s[98:99]
	s_add_u32 s98, s98, 0x2000
	s_addc_u32 s99, s99, 0
	global_load_dwordx4 v[52:55], v3, s[98:99]
	s_add_u32 s98, s98, 0x2000
	s_addc_u32 s99, s99, 0
	global_load_dwordx4 v[56:59], v3, s[98:99]
	s_add_u32 s98, s98, 0x2000
	s_addc_u32 s99, s99, 0
	global_load_dwordx4 v[60:63], v3, s[98:99]
	s_add_u32 s98, s98, 0x2000
	s_addc_u32 s99, s99, 0
	global_load_dwordx4 v[64:67], v3, s[98:99]
	v_add_u32_e32 v72, 0x10000, v1
	s_waitcnt vmcnt(15)
	ds_write_b128 v1, v[4:7]
	s_waitcnt vmcnt(14)
	ds_write_b128 v1, v[8:11] offset:8192
	s_waitcnt vmcnt(13)
	ds_write_b128 v1, v[12:15] offset:16384
	s_waitcnt vmcnt(12)
	ds_write_b128 v1, v[16:19] offset:24576
	s_waitcnt vmcnt(11)
	ds_write_b128 v1, v[20:23] offset:32768
	s_waitcnt vmcnt(10)
	ds_write_b128 v1, v[24:27] offset:40960
	s_waitcnt vmcnt(9)
	ds_write_b128 v1, v[28:31] offset:49152
	s_waitcnt vmcnt(8)
	ds_write_b128 v1, v[32:35] offset:57344
	s_waitcnt vmcnt(7)
	ds_write_b128 v72, v[36:39]
	s_waitcnt vmcnt(6)
	ds_write_b128 v72, v[40:43] offset:8192
	s_waitcnt vmcnt(5)
	ds_write_b128 v72, v[44:47] offset:16384
	s_waitcnt vmcnt(4)
	ds_write_b128 v72, v[48:51] offset:24576
	s_waitcnt vmcnt(3)
	ds_write_b128 v72, v[52:55] offset:32768
	s_waitcnt vmcnt(2)
	ds_write_b128 v72, v[56:59] offset:40960
	s_waitcnt vmcnt(1)
	ds_write_b128 v72, v[60:63] offset:49152
	s_waitcnt vmcnt(0)
	ds_write_b128 v72, v[64:67] offset:57344
	v_writelane_b32 v255, s84, 35
	v_cmp_gt_i32_e32 vcc, 64, v2
	s_nop 0
	v_writelane_b32 v255, s85, 36
	s_and_saveexec_b64 s[2:3], vcc
	s_cbranch_execz .LBB0_929
	v_add_u32_e32 v8, 0x2000, v2
	v_lshl_add_u32 v1, v8, 4, 0
	s_waitcnt vmcnt(0)
	ds_write_b128 v1, v[68:71]
